# gate/up LIVE1 K-loop: four fragment base addresses precomputed in v247..v250 and four gather-offset copies hoisted to the loop preheader (10 VALU fewer per iteration, 8 of them ahead of the 16-read se
# speedup vs baseline: 1.0080x; 1.0080x over previous
; template <class Epi, class Sched>
; __device__ __forceinline__ void gemm_phase(LAS unsigned char* lds, const Sched& S, const Epi& E) {
;     ...
; #pragma unroll
;         for (int a = 0; a < 2; ++a)
; #pragma unroll
;             for (int b = 0; b < 2; ++b)
; #pragma unroll
;                 for (int m = 0; m < 4; ++m)
; #pragma unroll
;                     for (int n = 0; n < 2; ++n) acc[a][b][m][n] = (f32x4){0.f, 0.f, 0.f, 0.f};
.LBB0_1242:
	v_mov_b32_e32 v117, 0
	s_and_b64 vcc, exec, s[18:19]
	v_mov_b32_e32 v116, v117
	v_mov_b32_e32 v115, v117
	v_mov_b32_e32 v114, v117
	v_mov_b32_e32 v101, v117
	v_mov_b32_e32 v100, v117
	v_mov_b32_e32 v99, v117
	v_mov_b32_e32 v98, v117
	v_mov_b32_e32 v85, v117
	v_mov_b32_e32 v84, v117
	v_mov_b32_e32 v83, v117
	v_mov_b32_e32 v82, v117
	s_waitcnt vmcnt(26)
	v_mov_b32_e32 v69, v117
	v_mov_b32_e32 v68, v117
	v_mov_b32_e32 v67, v117
	v_mov_b32_e32 v66, v117
	s_waitcnt vmcnt(23)
	v_mov_b32_e32 v53, v117
	v_mov_b32_e32 v52, v117
	v_mov_b32_e32 v51, v117
	v_mov_b32_e32 v50, v117
	v_mov_b32_e32 v37, v117
	v_mov_b32_e32 v36, v117
	v_mov_b32_e32 v35, v117
	v_mov_b32_e32 v34, v117
	v_mov_b32_e32 v21, v117
	v_mov_b32_e32 v20, v117
	v_mov_b32_e32 v19, v117
	v_mov_b32_e32 v18, v117
	v_mov_b32_e32 v9, v117
	v_mov_b32_e32 v8, v117
	v_mov_b32_e32 v7, v117
	v_mov_b32_e32 v6, v117
	v_mov_b32_e32 v109, v117
	v_mov_b32_e32 v108, v117
	v_mov_b32_e32 v107, v117
	v_mov_b32_e32 v106, v117
	v_mov_b32_e32 v97, v117
	v_mov_b32_e32 v96, v117
	v_mov_b32_e32 v95, v117
	v_mov_b32_e32 v94, v117
	v_mov_b32_e32 v81, v117
	v_mov_b32_e32 v80, v117
	v_mov_b32_e32 v79, v117
	v_mov_b32_e32 v78, v117
	s_waitcnt vmcnt(22)
	v_mov_b32_e32 v65, v117
	v_mov_b32_e32 v64, v117
	v_mov_b32_e32 v63, v117
	v_mov_b32_e32 v62, v117
	v_mov_b32_e32 v49, v117
	v_mov_b32_e32 v48, v117
	v_mov_b32_e32 v47, v117
	v_mov_b32_e32 v46, v117
	v_mov_b32_e32 v33, v117
	v_mov_b32_e32 v32, v117
	v_mov_b32_e32 v31, v117
	v_mov_b32_e32 v30, v117
	v_mov_b32_e32 v17, v117
	v_mov_b32_e32 v16, v117
	v_mov_b32_e32 v15, v117
	v_mov_b32_e32 v14, v117
	v_mov_b32_e32 v5, v117
	v_mov_b32_e32 v4, v117
	v_mov_b32_e32 v3, v117
	v_mov_b32_e32 v2, v117
	s_cbranch_vccz .LBB0_1248
	v_mov_b32_e32 v2, 0
	s_add_u32 s29, s38, 0x100
	s_mov_b32 s44, -2
	s_mov_b64 s[18:19], 0
	v_mov_b32_e32 v3, v2
	v_mov_b32_e32 v4, v2
	v_mov_b32_e32 v5, v2
	v_mov_b32_e32 v14, v2
	v_mov_b32_e32 v15, v2
	v_mov_b32_e32 v16, v2
	v_mov_b32_e32 v17, v2
	v_mov_b32_e32 v30, v2
	v_mov_b32_e32 v31, v2
	v_mov_b32_e32 v32, v2
	v_mov_b32_e32 v33, v2
	v_mov_b32_e32 v46, v2
	v_mov_b32_e32 v47, v2
	v_mov_b32_e32 v48, v2
	v_mov_b32_e32 v49, v2
	v_mov_b32_e32 v62, v2
	v_mov_b32_e32 v63, v2
	v_mov_b32_e32 v64, v2
	v_mov_b32_e32 v65, v2
	v_mov_b32_e32 v78, v2
	v_mov_b32_e32 v79, v2
	v_mov_b32_e32 v80, v2
	v_mov_b32_e32 v81, v2
	v_mov_b32_e32 v94, v2
	v_mov_b32_e32 v95, v2
	v_mov_b32_e32 v96, v2
	v_mov_b32_e32 v97, v2
	v_mov_b32_e32 v106, v2
	v_mov_b32_e32 v107, v2
	v_mov_b32_e32 v108, v2
	v_mov_b32_e32 v109, v2
	v_mov_b32_e32 v6, v2
	v_mov_b32_e32 v7, v2
	v_mov_b32_e32 v8, v2
	v_mov_b32_e32 v9, v2
	v_mov_b32_e32 v18, v2
	v_mov_b32_e32 v19, v2
	v_mov_b32_e32 v20, v2
	v_mov_b32_e32 v21, v2
	v_mov_b32_e32 v34, v2
	v_mov_b32_e32 v35, v2
	v_mov_b32_e32 v36, v2
	v_mov_b32_e32 v37, v2
	v_mov_b32_e32 v50, v2
	v_mov_b32_e32 v51, v2
	v_mov_b32_e32 v52, v2
	v_mov_b32_e32 v53, v2
	v_mov_b32_e32 v66, v2
	v_mov_b32_e32 v67, v2
	v_mov_b32_e32 v68, v2
	v_mov_b32_e32 v69, v2
	v_mov_b32_e32 v82, v2
	v_mov_b32_e32 v83, v2
	v_mov_b32_e32 v84, v2
	v_mov_b32_e32 v85, v2
	v_mov_b32_e32 v98, v2
	v_mov_b32_e32 v99, v2
	v_mov_b32_e32 v100, v2
	v_mov_b32_e32 v101, v2
	v_mov_b32_e32 v114, v2
	v_mov_b32_e32 v115, v2
	v_mov_b32_e32 v116, v2
	v_mov_b32_e32 v117, v2
	v_mov_b32_e32 v10, v2
	v_mov_b32_e32 v11, v2
	v_mov_b32_e32 v12, v2
	v_mov_b32_e32 v13, v2
	v_mov_b32_e32 v22, v2
	v_mov_b32_e32 v23, v2
	v_mov_b32_e32 v24, v2
	v_mov_b32_e32 v25, v2
	v_mov_b32_e32 v42, v2
	v_mov_b32_e32 v43, v2
	v_mov_b32_e32 v44, v2
	v_mov_b32_e32 v45, v2
	s_waitcnt vmcnt(21)
	v_mov_b32_e32 v54, v2
	v_mov_b32_e32 v55, v2
	v_mov_b32_e32 v56, v2
	v_mov_b32_e32 v57, v2
	v_mov_b32_e32 v74, v2
	v_mov_b32_e32 v75, v2
	v_mov_b32_e32 v76, v2
	v_mov_b32_e32 v77, v2
	v_mov_b32_e32 v86, v2
	v_mov_b32_e32 v87, v2
	v_mov_b32_e32 v88, v2
	v_mov_b32_e32 v89, v2
	v_mov_b32_e32 v110, v2
	v_mov_b32_e32 v111, v2
	v_mov_b32_e32 v112, v2
	v_mov_b32_e32 v113, v2
	v_mov_b32_e32 v118, v2
	v_mov_b32_e32 v119, v2
	v_mov_b32_e32 v120, v2
	v_mov_b32_e32 v121, v2
	v_mov_b32_e32 v26, v2
	v_mov_b32_e32 v27, v2
	v_mov_b32_e32 v28, v2
	v_mov_b32_e32 v29, v2
	v_mov_b32_e32 v38, v2
	v_mov_b32_e32 v39, v2
	v_mov_b32_e32 v40, v2
	v_mov_b32_e32 v41, v2
	v_mov_b32_e32 v58, v2
	v_mov_b32_e32 v59, v2
	v_mov_b32_e32 v60, v2
	v_mov_b32_e32 v61, v2
	v_mov_b32_e32 v70, v2
	v_mov_b32_e32 v71, v2
	v_mov_b32_e32 v72, v2
	v_mov_b32_e32 v73, v2
	v_mov_b32_e32 v90, v2
	v_mov_b32_e32 v91, v2
	v_mov_b32_e32 v92, v2
	v_mov_b32_e32 v93, v2
	v_mov_b32_e32 v102, v2
	v_mov_b32_e32 v103, v2
	v_mov_b32_e32 v104, v2
	v_mov_b32_e32 v105, v2
	v_mov_b32_e32 v122, v2
	v_mov_b32_e32 v123, v2
	v_mov_b32_e32 v124, v2
	v_mov_b32_e32 v125, v2
	v_mov_b32_e32 v126, v2
	v_mov_b32_e32 v127, v2
	v_mov_b32_e32 v128, v2
	v_mov_b32_e32 v129, v2
	v_mov_b32_e32 v139, v134
	v_mov_b32_e32 v140, v132
	v_mov_b32_e32 v137, v133
	v_mov_b32_e32 v138, v131
	v_add_u32_e32 v247, 0x10000, v157
	v_add_u32_e32 v248, 0x14000, v157
	v_add_u32_e32 v249, 0x18000, v157
	v_add_u32_e32 v250, 0x1c000, v157
.LBB0_1244:
	s_cmp_eq_u32 s44, 28
	s_cselect_b64 s[42:43], -1, 0
	s_cmp_lg_u32 s44, 28
	s_cbranch_scc1 .LBB0_1246
	ds_read_u16 v137, v135
	ds_read_u16 v139, v135 offset:256
	ds_read_u16 v141, v136
	ds_read_u16 v142, v136 offset:256
	s_waitcnt lgkmcnt(3)
	v_lshl_or_b32 v138, v137, 12, v147
	s_waitcnt lgkmcnt(2)
	v_lshl_or_b32 v140, v139, 12, v147
	s_waitcnt lgkmcnt(1)
	v_lshl_or_b32 v137, v141, 12, v147
	s_waitcnt lgkmcnt(0)
	v_lshl_or_b32 v139, v142, 12, v147
.LBB0_1246:
	ds_read_b128 v[142:145], v247
	ds_read_b128 v[172:175], v247 offset:1024
	ds_read_b128 v[176:179], v247 offset:2048
	ds_read_b128 v[180:183], v247 offset:3072
	ds_read_b128 v[184:187], v248
	ds_read_b128 v[188:191], v248 offset:1024
	ds_read_b128 v[196:199], v248 offset:2048
	ds_read_b128 v[200:203], v248 offset:3072
	s_add_u32 s38, s18, 0x100
	s_addc_u32 s39, s19, 0
	s_add_i32 s85, s29, s18
	s_and_b64 s[14:15], s[42:43], exec
	s_cselect_b32 s45, 0, s38
	s_add_i32 s14, s18, 0x80
	s_mov_b32 m0, s79
	ds_read_b128 v[204:207], v156
	ds_read_b128 v[208:211], v156 offset:1024
	ds_read_b128 v[212:215], v156 offset:2048
	ds_read_b128 v[216:219], v156 offset:3072
	ds_read_b128 v[220:223], v156 offset:4096
	ds_read_b128 v[224:227], v156 offset:5120
	ds_read_b128 v[228:231], v156 offset:6144
	ds_read_b128 v[232:235], v156 offset:7168
	buffer_load_dwordx4 v132, s[8:11], s14 offen lds
	s_mov_b32 m0, s80
	s_nop 0
	buffer_load_dwordx4 v134, s[8:11], s14 offen lds
	s_waitcnt vmcnt(8)
	s_waitcnt lgkmcnt(0)
	s_barrier
	v_mfma_f32_16x16x32_bf16 v[126:129], v[142:145], v[204:207], v[126:129]
	v_mfma_f32_16x16x32_bf16 v[122:125], v[176:179], v[204:207], v[122:125]
	v_mfma_f32_16x16x32_bf16 v[102:105], v[142:145], v[212:215], v[102:105]
	v_mfma_f32_16x16x32_bf16 v[90:93], v[176:179], v[212:215], v[90:93]
	v_mfma_f32_16x16x32_bf16 v[70:73], v[142:145], v[220:223], v[70:73]
	v_mfma_f32_16x16x32_bf16 v[58:61], v[176:179], v[220:223], v[58:61]
	v_mfma_f32_16x16x32_bf16 v[38:41], v[142:145], v[228:231], v[38:41]
	v_mfma_f32_16x16x32_bf16 v[26:29], v[176:179], v[228:231], v[26:29]
	v_mfma_f32_16x16x32_bf16 v[118:121], v[184:187], v[204:207], v[118:121]
	v_mfma_f32_16x16x32_bf16 v[110:113], v[196:199], v[204:207], v[110:113]
	v_mfma_f32_16x16x32_bf16 v[86:89], v[184:187], v[212:215], v[86:89]
	v_mfma_f32_16x16x32_bf16 v[74:77], v[196:199], v[212:215], v[74:77]
	v_mfma_f32_16x16x32_bf16 v[54:57], v[184:187], v[220:223], v[54:57]
	v_mfma_f32_16x16x32_bf16 v[42:45], v[196:199], v[220:223], v[42:45]
	v_mfma_f32_16x16x32_bf16 v[22:25], v[184:187], v[228:231], v[22:25]
	v_mfma_f32_16x16x32_bf16 v[10:13], v[196:199], v[228:231], v[10:13]
	v_mfma_f32_16x16x32_bf16 v[126:129], v[172:175], v[208:211], v[126:129]
	v_mfma_f32_16x16x32_bf16 v[122:125], v[180:183], v[208:211], v[122:125]
	v_mfma_f32_16x16x32_bf16 v[102:105], v[172:175], v[216:219], v[102:105]
	v_mfma_f32_16x16x32_bf16 v[90:93], v[180:183], v[216:219], v[90:93]
	v_mfma_f32_16x16x32_bf16 v[70:73], v[172:175], v[224:227], v[70:73]
	v_mfma_f32_16x16x32_bf16 v[58:61], v[180:183], v[224:227], v[58:61]
	v_mfma_f32_16x16x32_bf16 v[38:41], v[172:175], v[232:235], v[38:41]
	v_mfma_f32_16x16x32_bf16 v[26:29], v[180:183], v[232:235], v[26:29]
	v_mfma_f32_16x16x32_bf16 v[118:121], v[188:191], v[208:211], v[118:121]
	v_mfma_f32_16x16x32_bf16 v[110:113], v[200:203], v[208:211], v[110:113]
	v_mfma_f32_16x16x32_bf16 v[86:89], v[188:191], v[216:219], v[86:89]
	v_mfma_f32_16x16x32_bf16 v[74:77], v[200:203], v[216:219], v[74:77]
	v_mfma_f32_16x16x32_bf16 v[54:57], v[188:191], v[224:227], v[54:57]
	v_mfma_f32_16x16x32_bf16 v[42:45], v[200:203], v[224:227], v[42:45]
	v_mfma_f32_16x16x32_bf16 v[22:25], v[188:191], v[232:235], v[22:25]
	v_mfma_f32_16x16x32_bf16 v[10:13], v[200:203], v[232:235], v[10:13]
	s_barrier
	s_and_b64 s[14:15], s[42:43], exec
	s_cselect_b32 s14, s5, s85
	s_mov_b32 m0, s66
	s_mov_b32 s18, s10
	s_mov_b32 s19, s11
	s_sub_i32 s14, s14, s16
	ds_read_b128 v[204:207], v156 offset:16384
	ds_read_b128 v[208:211], v156 offset:17408
	ds_read_b128 v[212:215], v156 offset:18432
	ds_read_b128 v[216:219], v156 offset:19456
	ds_read_b128 v[220:223], v156 offset:20480
	ds_read_b128 v[224:227], v156 offset:21504
	ds_read_b128 v[228:231], v156 offset:22528
	ds_read_b128 v[232:235], v156 offset:23552
	buffer_load_dwordx4 v151, s[16:19], s14 offen lds
	s_mov_b32 m0, s67
	s_add_i32 s15, s14, 0x80000
	buffer_load_dwordx4 v158, s[16:19], s14 offen lds
	s_mov_b32 m0, s68
	s_nop 0
	buffer_load_dwordx4 v151, s[16:19], s15 offen lds
	s_mov_b32 m0, s69
	s_nop 0
	buffer_load_dwordx4 v158, s[16:19], s15 offen lds
	s_mov_b32 m0, s65
	s_nop 0
	buffer_load_dwordx4 v138, s[8:11], s45 offen lds
	s_mov_b32 m0, s70
	s_nop 0
	buffer_load_dwordx4 v137, s[8:11], s45 offen lds
	s_waitcnt vmcnt(8)
	s_waitcnt lgkmcnt(0)
	s_barrier
	v_mfma_f32_16x16x32_bf16 v[114:117], v[142:145], v[204:207], v[114:117]
	v_mfma_f32_16x16x32_bf16 v[98:101], v[176:179], v[204:207], v[98:101]
	v_mfma_f32_16x16x32_bf16 v[82:85], v[142:145], v[212:215], v[82:85]
	v_mfma_f32_16x16x32_bf16 v[66:69], v[176:179], v[212:215], v[66:69]
	v_mfma_f32_16x16x32_bf16 v[50:53], v[142:145], v[220:223], v[50:53]
	v_mfma_f32_16x16x32_bf16 v[34:37], v[176:179], v[220:223], v[34:37]
	v_mfma_f32_16x16x32_bf16 v[18:21], v[142:145], v[228:231], v[18:21]
	v_mfma_f32_16x16x32_bf16 v[6:9], v[176:179], v[228:231], v[6:9]
	v_mfma_f32_16x16x32_bf16 v[106:109], v[184:187], v[204:207], v[106:109]
	v_mfma_f32_16x16x32_bf16 v[94:97], v[196:199], v[204:207], v[94:97]
	v_mfma_f32_16x16x32_bf16 v[78:81], v[184:187], v[212:215], v[78:81]
	v_mfma_f32_16x16x32_bf16 v[62:65], v[196:199], v[212:215], v[62:65]
	v_mfma_f32_16x16x32_bf16 v[46:49], v[184:187], v[220:223], v[46:49]
	v_mfma_f32_16x16x32_bf16 v[30:33], v[196:199], v[220:223], v[30:33]
	v_mfma_f32_16x16x32_bf16 v[14:17], v[184:187], v[228:231], v[14:17]
	v_mfma_f32_16x16x32_bf16 v[2:5], v[196:199], v[228:231], v[2:5]
	v_mfma_f32_16x16x32_bf16 v[114:117], v[172:175], v[208:211], v[114:117]
	v_mfma_f32_16x16x32_bf16 v[98:101], v[180:183], v[208:211], v[98:101]
	v_mfma_f32_16x16x32_bf16 v[82:85], v[172:175], v[216:219], v[82:85]
	v_mfma_f32_16x16x32_bf16 v[66:69], v[180:183], v[216:219], v[66:69]
	v_mfma_f32_16x16x32_bf16 v[50:53], v[172:175], v[224:227], v[50:53]
	v_mfma_f32_16x16x32_bf16 v[34:37], v[180:183], v[224:227], v[34:37]
	v_mfma_f32_16x16x32_bf16 v[18:21], v[172:175], v[232:235], v[18:21]
	v_mfma_f32_16x16x32_bf16 v[6:9], v[180:183], v[232:235], v[6:9]
	v_mfma_f32_16x16x32_bf16 v[106:109], v[188:191], v[208:211], v[106:109]
	v_mfma_f32_16x16x32_bf16 v[94:97], v[200:203], v[208:211], v[94:97]
	v_mfma_f32_16x16x32_bf16 v[78:81], v[188:191], v[216:219], v[78:81]
	v_mfma_f32_16x16x32_bf16 v[62:65], v[200:203], v[216:219], v[62:65]
	v_mfma_f32_16x16x32_bf16 v[46:49], v[188:191], v[224:227], v[46:49]
	v_mfma_f32_16x16x32_bf16 v[30:33], v[200:203], v[224:227], v[30:33]
	v_mfma_f32_16x16x32_bf16 v[14:17], v[188:191], v[232:235], v[14:17]
	v_mfma_f32_16x16x32_bf16 v[2:5], v[200:203], v[232:235], v[2:5]
	s_barrier
	ds_read_b128 v[142:145], v249
	ds_read_b128 v[172:175], v249 offset:1024
	ds_read_b128 v[176:179], v249 offset:2048
	ds_read_b128 v[180:183], v249 offset:3072
	ds_read_b128 v[184:187], v250
	ds_read_b128 v[188:191], v250 offset:1024
	ds_read_b128 v[196:199], v250 offset:2048
	ds_read_b128 v[200:203], v250 offset:3072
	s_mov_b32 m0, s71
	ds_read_b128 v[204:207], v156 offset:32768
	ds_read_b128 v[208:211], v156 offset:33792
	ds_read_b128 v[212:215], v156 offset:34816
	ds_read_b128 v[216:219], v156 offset:35840
	ds_read_b128 v[220:223], v156 offset:36864
	ds_read_b128 v[224:227], v156 offset:37888
	ds_read_b128 v[228:231], v156 offset:38912
	ds_read_b128 v[232:235], v156 offset:39936
	buffer_load_dwordx4 v140, s[8:11], s45 offen lds
	s_mov_b32 m0, s72
	s_nop 0
	buffer_load_dwordx4 v139, s[8:11], s45 offen lds
	s_waitcnt vmcnt(8)
	s_waitcnt lgkmcnt(0)
	s_barrier
	v_mfma_f32_16x16x32_bf16 v[126:129], v[142:145], v[204:207], v[126:129]
	v_mfma_f32_16x16x32_bf16 v[122:125], v[176:179], v[204:207], v[122:125]
	v_mfma_f32_16x16x32_bf16 v[102:105], v[142:145], v[212:215], v[102:105]
	v_mfma_f32_16x16x32_bf16 v[90:93], v[176:179], v[212:215], v[90:93]
	v_mfma_f32_16x16x32_bf16 v[70:73], v[142:145], v[220:223], v[70:73]
	v_mfma_f32_16x16x32_bf16 v[58:61], v[176:179], v[220:223], v[58:61]
	v_mfma_f32_16x16x32_bf16 v[38:41], v[142:145], v[228:231], v[38:41]
	v_mfma_f32_16x16x32_bf16 v[26:29], v[176:179], v[228:231], v[26:29]
	v_mfma_f32_16x16x32_bf16 v[118:121], v[184:187], v[204:207], v[118:121]
	v_mfma_f32_16x16x32_bf16 v[110:113], v[196:199], v[204:207], v[110:113]
	v_mfma_f32_16x16x32_bf16 v[86:89], v[184:187], v[212:215], v[86:89]
	v_mfma_f32_16x16x32_bf16 v[74:77], v[196:199], v[212:215], v[74:77]
	v_mfma_f32_16x16x32_bf16 v[54:57], v[184:187], v[220:223], v[54:57]
	v_mfma_f32_16x16x32_bf16 v[42:45], v[196:199], v[220:223], v[42:45]
	v_mfma_f32_16x16x32_bf16 v[22:25], v[184:187], v[228:231], v[22:25]
	v_mfma_f32_16x16x32_bf16 v[10:13], v[196:199], v[228:231], v[10:13]
	v_mfma_f32_16x16x32_bf16 v[126:129], v[172:175], v[208:211], v[126:129]
	v_mfma_f32_16x16x32_bf16 v[122:125], v[180:183], v[208:211], v[122:125]
	v_mfma_f32_16x16x32_bf16 v[102:105], v[172:175], v[216:219], v[102:105]
	v_mfma_f32_16x16x32_bf16 v[90:93], v[180:183], v[216:219], v[90:93]
	v_mfma_f32_16x16x32_bf16 v[70:73], v[172:175], v[224:227], v[70:73]
	v_mfma_f32_16x16x32_bf16 v[58:61], v[180:183], v[224:227], v[58:61]
	v_mfma_f32_16x16x32_bf16 v[38:41], v[172:175], v[232:235], v[38:41]
	v_mfma_f32_16x16x32_bf16 v[26:29], v[180:183], v[232:235], v[26:29]
	v_mfma_f32_16x16x32_bf16 v[118:121], v[188:191], v[208:211], v[118:121]
	v_mfma_f32_16x16x32_bf16 v[110:113], v[200:203], v[208:211], v[110:113]
	v_mfma_f32_16x16x32_bf16 v[86:89], v[188:191], v[216:219], v[86:89]
	v_mfma_f32_16x16x32_bf16 v[74:77], v[200:203], v[216:219], v[74:77]
	v_mfma_f32_16x16x32_bf16 v[54:57], v[188:191], v[224:227], v[54:57]
	v_mfma_f32_16x16x32_bf16 v[42:45], v[200:203], v[224:227], v[42:45]
	v_mfma_f32_16x16x32_bf16 v[22:25], v[188:191], v[232:235], v[22:25]
	v_mfma_f32_16x16x32_bf16 v[10:13], v[200:203], v[232:235], v[10:13]
	s_barrier
	s_mov_b32 m0, s73
	s_add_i32 s15, s14, 0x80
	ds_read_b128 v[204:207], v156 offset:49152
	ds_read_b128 v[208:211], v156 offset:50176
	ds_read_b128 v[212:215], v156 offset:51200
	ds_read_b128 v[216:219], v156 offset:52224
	ds_read_b128 v[220:223], v156 offset:53248
	ds_read_b128 v[224:227], v156 offset:54272
	ds_read_b128 v[228:231], v156 offset:55296
	ds_read_b128 v[232:235], v156 offset:56320
	buffer_load_dwordx4 v151, s[16:19], s15 offen lds
	s_mov_b32 m0, s74
	s_add_i32 s14, s14, 0x80080
	buffer_load_dwordx4 v158, s[16:19], s15 offen lds
	s_mov_b32 m0, s77
	s_bitset1_b32 s45, 7
	buffer_load_dwordx4 v151, s[16:19], s14 offen lds
	s_mov_b32 m0, s78
	s_nop 0
	buffer_load_dwordx4 v158, s[16:19], s14 offen lds
	s_mov_b32 m0, s75
	s_nop 0
	buffer_load_dwordx4 v138, s[8:11], s45 offen lds
	s_mov_b32 m0, s76
	s_nop 0
	buffer_load_dwordx4 v137, s[8:11], s45 offen lds
	s_waitcnt vmcnt(8)
	s_waitcnt lgkmcnt(0)
	s_barrier
	v_mfma_f32_16x16x32_bf16 v[114:117], v[142:145], v[204:207], v[114:117]
	v_mfma_f32_16x16x32_bf16 v[98:101], v[176:179], v[204:207], v[98:101]
	v_mfma_f32_16x16x32_bf16 v[82:85], v[142:145], v[212:215], v[82:85]
	v_mfma_f32_16x16x32_bf16 v[66:69], v[176:179], v[212:215], v[66:69]
	v_mfma_f32_16x16x32_bf16 v[50:53], v[142:145], v[220:223], v[50:53]
	v_mfma_f32_16x16x32_bf16 v[34:37], v[176:179], v[220:223], v[34:37]
	v_mfma_f32_16x16x32_bf16 v[18:21], v[142:145], v[228:231], v[18:21]
	v_mfma_f32_16x16x32_bf16 v[6:9], v[176:179], v[228:231], v[6:9]
	v_mfma_f32_16x16x32_bf16 v[106:109], v[184:187], v[204:207], v[106:109]
	v_mfma_f32_16x16x32_bf16 v[94:97], v[196:199], v[204:207], v[94:97]
	v_mfma_f32_16x16x32_bf16 v[78:81], v[184:187], v[212:215], v[78:81]
	v_mfma_f32_16x16x32_bf16 v[62:65], v[196:199], v[212:215], v[62:65]
	v_mfma_f32_16x16x32_bf16 v[46:49], v[184:187], v[220:223], v[46:49]
	v_mfma_f32_16x16x32_bf16 v[30:33], v[196:199], v[220:223], v[30:33]
	v_mfma_f32_16x16x32_bf16 v[14:17], v[184:187], v[228:231], v[14:17]
	v_mfma_f32_16x16x32_bf16 v[2:5], v[196:199], v[228:231], v[2:5]
	v_mfma_f32_16x16x32_bf16 v[114:117], v[172:175], v[208:211], v[114:117]
	v_mfma_f32_16x16x32_bf16 v[98:101], v[180:183], v[208:211], v[98:101]
	v_mfma_f32_16x16x32_bf16 v[82:85], v[172:175], v[216:219], v[82:85]
	v_mfma_f32_16x16x32_bf16 v[66:69], v[180:183], v[216:219], v[66:69]
	v_mfma_f32_16x16x32_bf16 v[50:53], v[172:175], v[224:227], v[50:53]
	v_mfma_f32_16x16x32_bf16 v[34:37], v[180:183], v[224:227], v[34:37]
	v_mfma_f32_16x16x32_bf16 v[18:21], v[172:175], v[232:235], v[18:21]
	v_mfma_f32_16x16x32_bf16 v[6:9], v[180:183], v[232:235], v[6:9]
	v_mfma_f32_16x16x32_bf16 v[106:109], v[188:191], v[208:211], v[106:109]
	v_mfma_f32_16x16x32_bf16 v[94:97], v[200:203], v[208:211], v[94:97]
	v_mfma_f32_16x16x32_bf16 v[78:81], v[188:191], v[216:219], v[78:81]
	v_mfma_f32_16x16x32_bf16 v[62:65], v[200:203], v[216:219], v[62:65]
	v_mfma_f32_16x16x32_bf16 v[46:49], v[188:191], v[224:227], v[46:49]
	v_mfma_f32_16x16x32_bf16 v[30:33], v[200:203], v[224:227], v[30:33]
	v_mfma_f32_16x16x32_bf16 v[14:17], v[188:191], v[232:235], v[14:17]
	v_mfma_f32_16x16x32_bf16 v[2:5], v[200:203], v[232:235], v[2:5]
	s_barrier
	s_add_i32 s44, s44, 2
	s_cmp_gt_u32 s44, 29
	s_cbranch_scc1 .LBB0_1248
	s_mov_b64 s[18:19], s[38:39]
	s_branch .LBB0_1244
